# Hyena filter unit output layer on the f32 matrix core (v_mfma_f32_32x32x2_f32), results stored from the accumulator layout; on top of mod ring
# speedup vs baseline: 1.0140x; 1.0140x over previous
.LBB0_390:
	s_lshl_b64 s[4:5], s[10:11], 26
	v_readlane_b32 s6, v252, 35
	s_load_dwordx16 s[40:55], s[0:1], 0xc0
	s_add_u32 s6, s6, s4
	v_readlane_b32 s4, v252, 36
	s_addc_u32 s7, s4, s5
	s_lshl_b64 s[4:5], s[10:11], 20
	v_readlane_b32 s8, v252, 37
	v_readlane_b32 s9, v252, 38
	s_add_u32 s8, s8, s4
	s_addc_u32 s9, s9, s5
	s_lshl_b64 s[4:5], s[10:11], 18
	s_waitcnt lgkmcnt(0)
	s_add_u32 s4, s42, s4
	s_addc_u32 s5, s43, s5
	s_lshl_b32 s10, s20, 2
	s_add_u32 s6, s6, s10
	s_addc_u32 s7, s7, 0
	s_lshl_b32 s10, s36, 2
	s_add_u32 s8, s8, s10
	s_addc_u32 s9, s9, 0
	s_add_i32 s23, s20, 0xffffe000
	s_mov_b64 exec, -1
	v_lshrrev_b32_e32 v2, 6, v0
	v_and_b32_e32 v3, 63, v0
	v_readfirstlane_b32 s31, v2
	v_lshrrev_b32_e32 v4, 5, v3
	v_and_b32_e32 v5, 31, v3
	s_lshl_b32 s10, s31, 9
	s_add_u32 s24, s4, s10
	s_addc_u32 s25, s5, 0
	s_lshl_b32 s10, s31, 23
	s_add_u32 s26, s6, s10
	s_addc_u32 s27, s7, 0
	s_lshl_b32 s10, s31, 17
	s_add_u32 s28, s8, s10
	s_addc_u32 s29, s9, 0
	v_lshlrev_b32_e32 v6, 2, v5
	v_lshl_add_u32 v8, v4, 17, v6
	v_lshl_add_u32 v9, v4, 18, v6
	v_add_u32_e32 v10, 0x80, v9
	v_lshlrev_b32_e32 v76, 12, v4
	v_add_u32_e32 v6, s23, v5
	v_cvt_f32_i32_e32 v77, v6
	v_mul_f32_e64 v77, |v77|, s22
	v_add_u32_e32 v6, 32, v6
	v_cvt_f32_i32_e32 v158, v6
	v_mul_f32_e64 v158, |v158|, s22
	s_lshl_b32 s10, s31, 7
	v_lshl_add_u32 v6, v4, 2, s10
	v_cvt_f32_i32_e32 v159, v6
	v_mul_u32_u24_e32 v6, 0x110, v5
	v_lshl_add_u32 v160, v4, 7, v6
	v_add_u32_e32 v160, 0x2400, v160
	s_mov_b32 s34, 0x80000000
	s_mov_b32 s35, 0x80000000
	s_mov_b32 s40, s24
	s_mov_b32 s41, s25
	global_load_dword v126, v8, s[40:41]
	s_add_u32 s40, s40, 0x1000
	s_addc_u32 s41, s41, 0
	global_load_dword v127, v8, s[40:41]
	s_add_u32 s40, s40, 0x1000
	s_addc_u32 s41, s41, 0
	global_load_dword v128, v8, s[40:41]
	s_add_u32 s40, s40, 0x1000
	s_addc_u32 s41, s41, 0
	global_load_dword v129, v8, s[40:41]
	s_add_u32 s40, s40, 0x1000
	s_addc_u32 s41, s41, 0
	global_load_dword v130, v8, s[40:41]
	s_add_u32 s40, s40, 0x1000
	s_addc_u32 s41, s41, 0
	global_load_dword v131, v8, s[40:41]
	s_add_u32 s40, s40, 0x1000
	s_addc_u32 s41, s41, 0
	global_load_dword v132, v8, s[40:41]
	s_add_u32 s40, s40, 0x1000
	s_addc_u32 s41, s41, 0
	global_load_dword v133, v8, s[40:41]
	s_add_u32 s40, s40, 0x1000
	s_addc_u32 s41, s41, 0
	global_load_dword v134, v8, s[40:41]
	s_add_u32 s40, s40, 0x1000
	s_addc_u32 s41, s41, 0
	global_load_dword v135, v8, s[40:41]
	s_add_u32 s40, s40, 0x1000
	s_addc_u32 s41, s41, 0
	global_load_dword v136, v8, s[40:41]
	s_add_u32 s40, s40, 0x1000
	s_addc_u32 s41, s41, 0
	global_load_dword v137, v8, s[40:41]
	s_add_u32 s40, s40, 0x1000
	s_addc_u32 s41, s41, 0
	global_load_dword v138, v8, s[40:41]
	s_add_u32 s40, s40, 0x1000
	s_addc_u32 s41, s41, 0
	global_load_dword v139, v8, s[40:41]
	s_add_u32 s40, s40, 0x1000
	s_addc_u32 s41, s41, 0
	global_load_dword v140, v8, s[40:41]
	s_add_u32 s40, s40, 0x1000
	s_addc_u32 s41, s41, 0
	global_load_dword v141, v8, s[40:41]
	s_add_u32 s40, s40, 0x1000
	s_addc_u32 s41, s41, 0
	global_load_dword v142, v8, s[40:41]
	s_add_u32 s40, s40, 0x1000
	s_addc_u32 s41, s41, 0
	global_load_dword v143, v8, s[40:41]
	s_add_u32 s40, s40, 0x1000
	s_addc_u32 s41, s41, 0
	global_load_dword v144, v8, s[40:41]
	s_add_u32 s40, s40, 0x1000
	s_addc_u32 s41, s41, 0
	global_load_dword v145, v8, s[40:41]
	s_add_u32 s40, s40, 0x1000
	s_addc_u32 s41, s41, 0
	global_load_dword v146, v8, s[40:41]
	s_add_u32 s40, s40, 0x1000
	s_addc_u32 s41, s41, 0
	global_load_dword v147, v8, s[40:41]
	s_add_u32 s40, s40, 0x1000
	s_addc_u32 s41, s41, 0
	global_load_dword v148, v8, s[40:41]
	s_add_u32 s40, s40, 0x1000
	s_addc_u32 s41, s41, 0
	global_load_dword v149, v8, s[40:41]
	s_add_u32 s40, s40, 0x1000
	s_addc_u32 s41, s41, 0
	global_load_dword v150, v8, s[40:41]
	s_add_u32 s40, s40, 0x1000
	s_addc_u32 s41, s41, 0
	global_load_dword v151, v8, s[40:41]
	s_add_u32 s40, s40, 0x1000
	s_addc_u32 s41, s41, 0
	global_load_dword v152, v8, s[40:41]
	s_add_u32 s40, s40, 0x1000
	s_addc_u32 s41, s41, 0
	global_load_dword v153, v8, s[40:41]
	s_add_u32 s40, s40, 0x1000
	s_addc_u32 s41, s41, 0
	global_load_dword v154, v8, s[40:41]
	s_add_u32 s40, s40, 0x1000
	s_addc_u32 s41, s41, 0
	global_load_dword v155, v8, s[40:41]
	s_add_u32 s40, s40, 0x1000
	s_addc_u32 s41, s41, 0
	global_load_dword v156, v8, s[40:41]
	s_add_u32 s40, s40, 0x1000
	s_addc_u32 s41, s41, 0
	global_load_dword v157, v8, s[40:41]
	s_add_u32 s40, s40, 0x1000
	s_addc_u32 s41, s41, 0
	s_add_u32 s24, s24, 0x80
	s_addc_u32 s25, s25, 0
	s_waitcnt lgkmcnt(0)
	s_barrier
	ds_read_b128 v[12:15], v160 offset:0
	ds_read_b128 v[44:47], v160 offset:8704
	ds_read_b128 v[16:19], v160 offset:16
	ds_read_b128 v[48:51], v160 offset:8720
	ds_read_b128 v[20:23], v160 offset:32
	ds_read_b128 v[52:55], v160 offset:8736
	ds_read_b128 v[24:27], v160 offset:48
	ds_read_b128 v[56:59], v160 offset:8752
	ds_read_b128 v[28:31], v160 offset:64
	ds_read_b128 v[60:63], v160 offset:8768
	ds_read_b128 v[32:35], v160 offset:80
	ds_read_b128 v[64:67], v160 offset:8784
	ds_read_b128 v[36:39], v160 offset:96
	ds_read_b128 v[68:71], v160 offset:8800
	ds_read_b128 v[40:43], v160 offset:112
	ds_read_b128 v[72:75], v160 offset:8816
	s_mov_b32 s30, 0
	s_waitcnt vmcnt(0) lgkmcnt(0)
.Lhf_blk:
	v_mfma_f32_32x32x2_f32 v[94:109], v126, v12, 0
	v_mfma_f32_32x32x2_f32 v[110:125], v126, v44, 0
	v_mfma_f32_32x32x2_f32 v[94:109], v127, v13, v[94:109]
	v_mfma_f32_32x32x2_f32 v[110:125], v127, v45, v[110:125]
	v_mfma_f32_32x32x2_f32 v[94:109], v128, v14, v[94:109]
	v_mfma_f32_32x32x2_f32 v[110:125], v128, v46, v[110:125]
	v_mfma_f32_32x32x2_f32 v[94:109], v129, v15, v[94:109]
	v_mfma_f32_32x32x2_f32 v[110:125], v129, v47, v[110:125]
	v_mfma_f32_32x32x2_f32 v[94:109], v130, v16, v[94:109]
	v_mfma_f32_32x32x2_f32 v[110:125], v130, v48, v[110:125]
	v_mfma_f32_32x32x2_f32 v[94:109], v131, v17, v[94:109]
	v_mfma_f32_32x32x2_f32 v[110:125], v131, v49, v[110:125]
	v_mfma_f32_32x32x2_f32 v[94:109], v132, v18, v[94:109]
	v_mfma_f32_32x32x2_f32 v[110:125], v132, v50, v[110:125]
	v_mfma_f32_32x32x2_f32 v[94:109], v133, v19, v[94:109]
	v_mfma_f32_32x32x2_f32 v[110:125], v133, v51, v[110:125]
	v_mfma_f32_32x32x2_f32 v[94:109], v134, v20, v[94:109]
	v_mfma_f32_32x32x2_f32 v[110:125], v134, v52, v[110:125]
	v_mfma_f32_32x32x2_f32 v[94:109], v135, v21, v[94:109]
	v_mfma_f32_32x32x2_f32 v[110:125], v135, v53, v[110:125]
	v_mfma_f32_32x32x2_f32 v[94:109], v136, v22, v[94:109]
	v_mfma_f32_32x32x2_f32 v[110:125], v136, v54, v[110:125]
	v_mfma_f32_32x32x2_f32 v[94:109], v137, v23, v[94:109]
	v_mfma_f32_32x32x2_f32 v[110:125], v137, v55, v[110:125]
	v_mfma_f32_32x32x2_f32 v[94:109], v138, v24, v[94:109]
	v_mfma_f32_32x32x2_f32 v[110:125], v138, v56, v[110:125]
	v_mfma_f32_32x32x2_f32 v[94:109], v139, v25, v[94:109]
	v_mfma_f32_32x32x2_f32 v[110:125], v139, v57, v[110:125]
	v_mfma_f32_32x32x2_f32 v[94:109], v140, v26, v[94:109]
	v_mfma_f32_32x32x2_f32 v[110:125], v140, v58, v[110:125]
	v_mfma_f32_32x32x2_f32 v[94:109], v141, v27, v[94:109]
	v_mfma_f32_32x32x2_f32 v[110:125], v141, v59, v[110:125]
	v_mfma_f32_32x32x2_f32 v[94:109], v142, v28, v[94:109]
	v_mfma_f32_32x32x2_f32 v[110:125], v142, v60, v[110:125]
	v_mfma_f32_32x32x2_f32 v[94:109], v143, v29, v[94:109]
	v_mfma_f32_32x32x2_f32 v[110:125], v143, v61, v[110:125]
	v_mfma_f32_32x32x2_f32 v[94:109], v144, v30, v[94:109]
	v_mfma_f32_32x32x2_f32 v[110:125], v144, v62, v[110:125]
	v_mfma_f32_32x32x2_f32 v[94:109], v145, v31, v[94:109]
	v_mfma_f32_32x32x2_f32 v[110:125], v145, v63, v[110:125]
	v_mfma_f32_32x32x2_f32 v[94:109], v146, v32, v[94:109]
	v_mfma_f32_32x32x2_f32 v[110:125], v146, v64, v[110:125]
	v_mfma_f32_32x32x2_f32 v[94:109], v147, v33, v[94:109]
	v_mfma_f32_32x32x2_f32 v[110:125], v147, v65, v[110:125]
	v_mfma_f32_32x32x2_f32 v[94:109], v148, v34, v[94:109]
	v_mfma_f32_32x32x2_f32 v[110:125], v148, v66, v[110:125]
	v_mfma_f32_32x32x2_f32 v[94:109], v149, v35, v[94:109]
	v_mfma_f32_32x32x2_f32 v[110:125], v149, v67, v[110:125]
	v_mfma_f32_32x32x2_f32 v[94:109], v150, v36, v[94:109]
	v_mfma_f32_32x32x2_f32 v[110:125], v150, v68, v[110:125]
	v_mfma_f32_32x32x2_f32 v[94:109], v151, v37, v[94:109]
	v_mfma_f32_32x32x2_f32 v[110:125], v151, v69, v[110:125]
	v_mfma_f32_32x32x2_f32 v[94:109], v152, v38, v[94:109]
	v_mfma_f32_32x32x2_f32 v[110:125], v152, v70, v[110:125]
	v_mfma_f32_32x32x2_f32 v[94:109], v153, v39, v[94:109]
	v_mfma_f32_32x32x2_f32 v[110:125], v153, v71, v[110:125]
	v_mfma_f32_32x32x2_f32 v[94:109], v154, v40, v[94:109]
	v_mfma_f32_32x32x2_f32 v[110:125], v154, v72, v[110:125]
	v_mfma_f32_32x32x2_f32 v[94:109], v155, v41, v[94:109]
	v_mfma_f32_32x32x2_f32 v[110:125], v155, v73, v[110:125]
	v_mfma_f32_32x32x2_f32 v[94:109], v156, v42, v[94:109]
	v_mfma_f32_32x32x2_f32 v[110:125], v156, v74, v[110:125]
	v_mfma_f32_32x32x2_f32 v[94:109], v157, v43, v[94:109]
	v_mfma_f32_32x32x2_f32 v[110:125], v157, v75, v[110:125]
	s_cmp_eq_u32 s30, 3
	s_cbranch_scc1 .Lhf_noload
	s_mov_b32 s40, s24
	s_mov_b32 s41, s25
	global_load_dword v126, v8, s[40:41]
	s_add_u32 s40, s40, 0x1000
	s_addc_u32 s41, s41, 0
	global_load_dword v127, v8, s[40:41]
	s_add_u32 s40, s40, 0x1000
	s_addc_u32 s41, s41, 0
	global_load_dword v128, v8, s[40:41]
	s_add_u32 s40, s40, 0x1000
	s_addc_u32 s41, s41, 0
	global_load_dword v129, v8, s[40:41]
	s_add_u32 s40, s40, 0x1000
	s_addc_u32 s41, s41, 0
	global_load_dword v130, v8, s[40:41]
	s_add_u32 s40, s40, 0x1000
	s_addc_u32 s41, s41, 0
	global_load_dword v131, v8, s[40:41]
	s_add_u32 s40, s40, 0x1000
	s_addc_u32 s41, s41, 0
	global_load_dword v132, v8, s[40:41]
	s_add_u32 s40, s40, 0x1000
	s_addc_u32 s41, s41, 0
	global_load_dword v133, v8, s[40:41]
	s_add_u32 s40, s40, 0x1000
	s_addc_u32 s41, s41, 0
	global_load_dword v134, v8, s[40:41]
	s_add_u32 s40, s40, 0x1000
	s_addc_u32 s41, s41, 0
	global_load_dword v135, v8, s[40:41]
	s_add_u32 s40, s40, 0x1000
	s_addc_u32 s41, s41, 0
	global_load_dword v136, v8, s[40:41]
	s_add_u32 s40, s40, 0x1000
	s_addc_u32 s41, s41, 0
	global_load_dword v137, v8, s[40:41]
	s_add_u32 s40, s40, 0x1000
	s_addc_u32 s41, s41, 0
	global_load_dword v138, v8, s[40:41]
	s_add_u32 s40, s40, 0x1000
	s_addc_u32 s41, s41, 0
	global_load_dword v139, v8, s[40:41]
	s_add_u32 s40, s40, 0x1000
	s_addc_u32 s41, s41, 0
	global_load_dword v140, v8, s[40:41]
	s_add_u32 s40, s40, 0x1000
	s_addc_u32 s41, s41, 0
	global_load_dword v141, v8, s[40:41]
	s_add_u32 s40, s40, 0x1000
	s_addc_u32 s41, s41, 0
	global_load_dword v142, v8, s[40:41]
	s_add_u32 s40, s40, 0x1000
	s_addc_u32 s41, s41, 0
	global_load_dword v143, v8, s[40:41]
	s_add_u32 s40, s40, 0x1000
	s_addc_u32 s41, s41, 0
	global_load_dword v144, v8, s[40:41]
	s_add_u32 s40, s40, 0x1000
	s_addc_u32 s41, s41, 0
	global_load_dword v145, v8, s[40:41]
	s_add_u32 s40, s40, 0x1000
	s_addc_u32 s41, s41, 0
	global_load_dword v146, v8, s[40:41]
	s_add_u32 s40, s40, 0x1000
	s_addc_u32 s41, s41, 0
	global_load_dword v147, v8, s[40:41]
	s_add_u32 s40, s40, 0x1000
	s_addc_u32 s41, s41, 0
	global_load_dword v148, v8, s[40:41]
	s_add_u32 s40, s40, 0x1000
	s_addc_u32 s41, s41, 0
	global_load_dword v149, v8, s[40:41]
	s_add_u32 s40, s40, 0x1000
	s_addc_u32 s41, s41, 0
	global_load_dword v150, v8, s[40:41]
	s_add_u32 s40, s40, 0x1000
	s_addc_u32 s41, s41, 0
	global_load_dword v151, v8, s[40:41]
	s_add_u32 s40, s40, 0x1000
	s_addc_u32 s41, s41, 0
	global_load_dword v152, v8, s[40:41]
	s_add_u32 s40, s40, 0x1000
	s_addc_u32 s41, s41, 0
	global_load_dword v153, v8, s[40:41]
	s_add_u32 s40, s40, 0x1000
	s_addc_u32 s41, s41, 0
	global_load_dword v154, v8, s[40:41]
	s_add_u32 s40, s40, 0x1000
	s_addc_u32 s41, s41, 0
	global_load_dword v155, v8, s[40:41]
	s_add_u32 s40, s40, 0x1000
	s_addc_u32 s41, s41, 0
	global_load_dword v156, v8, s[40:41]
	s_add_u32 s40, s40, 0x1000
	s_addc_u32 s41, s41, 0
	global_load_dword v157, v8, s[40:41]
	s_add_u32 s40, s40, 0x1000
	s_addc_u32 s41, s41, 0
	s_add_u32 s24, s24, 0x80
	s_addc_u32 s25, s25, 0
.Lhf_noload:
	s_nop 15
	s_nop 7
	s_mov_b32 s44, s26
	s_mov_b32 s45, s27
	v_add_f32_e32 v2, 0, v159
	v_fmamk_f32 v2, v2, 0x3e2119e2, v80
	v_mul_f32_e64 v3, |v2|, v77
	v_mul_f32_e32 v4, 0x3fb8aa3b, v3
	v_fma_f32 v5, v3, s95, -v4
	v_rndne_f32_e32 v6, v4
	v_fmac_f32_e32 v5, 0x32a5705f, v3
	v_sub_f32_e32 v4, v4, v6
	v_add_f32_e32 v4, v4, v5
	v_exp_f32_e32 v4, v4
	v_cvt_i32_f32_e32 v6, v6
	v_cmp_ngt_f32_e32 vcc, s96, v3
	v_ldexp_f32 v4, v4, v6
	s_nop 0
	v_cndmask_b32_e32 v4, 0, v4, vcc
	v_cmp_nlt_f32_e32 vcc, s97, v3
	s_nop 1
	v_cndmask_b32_e32 v4, v93, v4, vcc
	v_mul_f32_e32 v4, v4, v94
	global_store_dword v9, v4, s[44:45]
	v_mul_f32_e64 v3, |v2|, v158
	v_mul_f32_e32 v7, 0x3fb8aa3b, v3
	v_fma_f32 v5, v3, s95, -v7
	v_rndne_f32_e32 v6, v7
	v_fmac_f32_e32 v5, 0x32a5705f, v3
	v_sub_f32_e32 v7, v7, v6
	v_add_f32_e32 v7, v7, v5
	v_exp_f32_e32 v7, v7
	v_cvt_i32_f32_e32 v6, v6
	v_cmp_ngt_f32_e32 vcc, s96, v3
	v_ldexp_f32 v7, v7, v6
	s_nop 0
	v_cndmask_b32_e32 v7, 0, v7, vcc
	v_cmp_nlt_f32_e32 vcc, s97, v3
	s_nop 1
	v_cndmask_b32_e32 v7, v93, v7, vcc
	v_mul_f32_e32 v7, v7, v110
	global_store_dword v10, v7, s[44:45]
	v_add_f32_e64 v94, |v4|, |v7|
	s_add_u32 s44, s44, 0x10000
	s_addc_u32 s45, s45, 0
	v_add_f32_e32 v2, 0x3f800000, v159
	v_fmamk_f32 v2, v2, 0x3e2119e2, v80
	v_mul_f32_e64 v3, |v2|, v77
	v_mul_f32_e32 v4, 0x3fb8aa3b, v3
	v_fma_f32 v5, v3, s95, -v4
	v_rndne_f32_e32 v6, v4
	v_fmac_f32_e32 v5, 0x32a5705f, v3
	v_sub_f32_e32 v4, v4, v6
	v_add_f32_e32 v4, v4, v5
	v_exp_f32_e32 v4, v4
	v_cvt_i32_f32_e32 v6, v6
	v_cmp_ngt_f32_e32 vcc, s96, v3
	v_ldexp_f32 v4, v4, v6
	s_nop 0
	v_cndmask_b32_e32 v4, 0, v4, vcc
	v_cmp_nlt_f32_e32 vcc, s97, v3
	s_nop 1
	v_cndmask_b32_e32 v4, v93, v4, vcc
	v_mul_f32_e32 v4, v4, v95
	global_store_dword v9, v4, s[44:45]
	v_mul_f32_e64 v3, |v2|, v158
	v_mul_f32_e32 v7, 0x3fb8aa3b, v3
	v_fma_f32 v5, v3, s95, -v7
	v_rndne_f32_e32 v6, v7
	v_fmac_f32_e32 v5, 0x32a5705f, v3
	v_sub_f32_e32 v7, v7, v6
	v_add_f32_e32 v7, v7, v5
	v_exp_f32_e32 v7, v7
	v_cvt_i32_f32_e32 v6, v6
	v_cmp_ngt_f32_e32 vcc, s96, v3
	v_ldexp_f32 v7, v7, v6
	s_nop 0
	v_cndmask_b32_e32 v7, 0, v7, vcc
	v_cmp_nlt_f32_e32 vcc, s97, v3
	s_nop 1
	v_cndmask_b32_e32 v7, v93, v7, vcc
	v_mul_f32_e32 v7, v7, v111
	global_store_dword v10, v7, s[44:45]
	v_add_f32_e64 v95, |v4|, |v7|
	s_add_u32 s44, s44, 0x10000
	s_addc_u32 s45, s45, 0
	v_add_f32_e32 v2, 0x40000000, v159
	v_fmamk_f32 v2, v2, 0x3e2119e2, v80
	v_mul_f32_e64 v3, |v2|, v77
	v_mul_f32_e32 v4, 0x3fb8aa3b, v3
	v_fma_f32 v5, v3, s95, -v4
	v_rndne_f32_e32 v6, v4
	v_fmac_f32_e32 v5, 0x32a5705f, v3
	v_sub_f32_e32 v4, v4, v6
	v_add_f32_e32 v4, v4, v5
	v_exp_f32_e32 v4, v4
	v_cvt_i32_f32_e32 v6, v6
	v_cmp_ngt_f32_e32 vcc, s96, v3
	v_ldexp_f32 v4, v4, v6
	s_nop 0
	v_cndmask_b32_e32 v4, 0, v4, vcc
	v_cmp_nlt_f32_e32 vcc, s97, v3
	s_nop 1
	v_cndmask_b32_e32 v4, v93, v4, vcc
	v_mul_f32_e32 v4, v4, v96
	global_store_dword v9, v4, s[44:45]
	v_mul_f32_e64 v3, |v2|, v158
	v_mul_f32_e32 v7, 0x3fb8aa3b, v3
	v_fma_f32 v5, v3, s95, -v7
	v_rndne_f32_e32 v6, v7
	v_fmac_f32_e32 v5, 0x32a5705f, v3
	v_sub_f32_e32 v7, v7, v6
	v_add_f32_e32 v7, v7, v5
	v_exp_f32_e32 v7, v7
	v_cvt_i32_f32_e32 v6, v6
	v_cmp_ngt_f32_e32 vcc, s96, v3
	v_ldexp_f32 v7, v7, v6
	s_nop 0
	v_cndmask_b32_e32 v7, 0, v7, vcc
	v_cmp_nlt_f32_e32 vcc, s97, v3
	s_nop 1
	v_cndmask_b32_e32 v7, v93, v7, vcc
	v_mul_f32_e32 v7, v7, v112
	global_store_dword v10, v7, s[44:45]
	v_add_f32_e64 v96, |v4|, |v7|
	s_add_u32 s44, s44, 0x10000
	s_addc_u32 s45, s45, 0
	v_add_f32_e32 v2, 0x40400000, v159
	v_fmamk_f32 v2, v2, 0x3e2119e2, v80
	v_mul_f32_e64 v3, |v2|, v77
	v_mul_f32_e32 v4, 0x3fb8aa3b, v3
	v_fma_f32 v5, v3, s95, -v4
	v_rndne_f32_e32 v6, v4
	v_fmac_f32_e32 v5, 0x32a5705f, v3
	v_sub_f32_e32 v4, v4, v6
	v_add_f32_e32 v4, v4, v5
	v_exp_f32_e32 v4, v4
	v_cvt_i32_f32_e32 v6, v6
	v_cmp_ngt_f32_e32 vcc, s96, v3
	v_ldexp_f32 v4, v4, v6
	s_nop 0
	v_cndmask_b32_e32 v4, 0, v4, vcc
	v_cmp_nlt_f32_e32 vcc, s97, v3
	s_nop 1
	v_cndmask_b32_e32 v4, v93, v4, vcc
	v_mul_f32_e32 v4, v4, v97
	global_store_dword v9, v4, s[44:45]
	v_mul_f32_e64 v3, |v2|, v158
	v_mul_f32_e32 v7, 0x3fb8aa3b, v3
	v_fma_f32 v5, v3, s95, -v7
	v_rndne_f32_e32 v6, v7
	v_fmac_f32_e32 v5, 0x32a5705f, v3
	v_sub_f32_e32 v7, v7, v6
	v_add_f32_e32 v7, v7, v5
	v_exp_f32_e32 v7, v7
	v_cvt_i32_f32_e32 v6, v6
	v_cmp_ngt_f32_e32 vcc, s96, v3
	v_ldexp_f32 v7, v7, v6
	s_nop 0
	v_cndmask_b32_e32 v7, 0, v7, vcc
	v_cmp_nlt_f32_e32 vcc, s97, v3
	s_nop 1
	v_cndmask_b32_e32 v7, v93, v7, vcc
	v_mul_f32_e32 v7, v7, v113
	global_store_dword v10, v7, s[44:45]
	v_add_f32_e64 v97, |v4|, |v7|
	s_add_u32 s44, s44, 0x50000
	s_addc_u32 s45, s45, 0
	v_add_f32_e32 v2, 0x41000000, v159
	v_fmamk_f32 v2, v2, 0x3e2119e2, v80
	v_mul_f32_e64 v3, |v2|, v77
	v_mul_f32_e32 v4, 0x3fb8aa3b, v3
	v_fma_f32 v5, v3, s95, -v4
	v_rndne_f32_e32 v6, v4
	v_fmac_f32_e32 v5, 0x32a5705f, v3
	v_sub_f32_e32 v4, v4, v6
	v_add_f32_e32 v4, v4, v5
	v_exp_f32_e32 v4, v4
	v_cvt_i32_f32_e32 v6, v6
	v_cmp_ngt_f32_e32 vcc, s96, v3
	v_ldexp_f32 v4, v4, v6
	s_nop 0
	v_cndmask_b32_e32 v4, 0, v4, vcc
	v_cmp_nlt_f32_e32 vcc, s97, v3
	s_nop 1
	v_cndmask_b32_e32 v4, v93, v4, vcc
	v_mul_f32_e32 v4, v4, v98
	global_store_dword v9, v4, s[44:45]
	v_mul_f32_e64 v3, |v2|, v158
	v_mul_f32_e32 v7, 0x3fb8aa3b, v3
	v_fma_f32 v5, v3, s95, -v7
	v_rndne_f32_e32 v6, v7
	v_fmac_f32_e32 v5, 0x32a5705f, v3
	v_sub_f32_e32 v7, v7, v6
	v_add_f32_e32 v7, v7, v5
	v_exp_f32_e32 v7, v7
	v_cvt_i32_f32_e32 v6, v6
	v_cmp_ngt_f32_e32 vcc, s96, v3
	v_ldexp_f32 v7, v7, v6
	s_nop 0
	v_cndmask_b32_e32 v7, 0, v7, vcc
	v_cmp_nlt_f32_e32 vcc, s97, v3
	s_nop 1
	v_cndmask_b32_e32 v7, v93, v7, vcc
	v_mul_f32_e32 v7, v7, v114
	global_store_dword v10, v7, s[44:45]
	v_add_f32_e64 v98, |v4|, |v7|
	s_add_u32 s44, s44, 0x10000
	s_addc_u32 s45, s45, 0
	v_add_f32_e32 v2, 0x41100000, v159
	v_fmamk_f32 v2, v2, 0x3e2119e2, v80
	v_mul_f32_e64 v3, |v2|, v77
	v_mul_f32_e32 v4, 0x3fb8aa3b, v3
	v_fma_f32 v5, v3, s95, -v4
	v_rndne_f32_e32 v6, v4
	v_fmac_f32_e32 v5, 0x32a5705f, v3
	v_sub_f32_e32 v4, v4, v6
	v_add_f32_e32 v4, v4, v5
	v_exp_f32_e32 v4, v4
	v_cvt_i32_f32_e32 v6, v6
	v_cmp_ngt_f32_e32 vcc, s96, v3
	v_ldexp_f32 v4, v4, v6
	s_nop 0
	v_cndmask_b32_e32 v4, 0, v4, vcc
	v_cmp_nlt_f32_e32 vcc, s97, v3
	s_nop 1
	v_cndmask_b32_e32 v4, v93, v4, vcc
	v_mul_f32_e32 v4, v4, v99
	global_store_dword v9, v4, s[44:45]
	v_mul_f32_e64 v3, |v2|, v158
	v_mul_f32_e32 v7, 0x3fb8aa3b, v3
	v_fma_f32 v5, v3, s95, -v7
	v_rndne_f32_e32 v6, v7
	v_fmac_f32_e32 v5, 0x32a5705f, v3
	v_sub_f32_e32 v7, v7, v6
	v_add_f32_e32 v7, v7, v5
	v_exp_f32_e32 v7, v7
	v_cvt_i32_f32_e32 v6, v6
	v_cmp_ngt_f32_e32 vcc, s96, v3
	v_ldexp_f32 v7, v7, v6
	s_nop 0
	v_cndmask_b32_e32 v7, 0, v7, vcc
	v_cmp_nlt_f32_e32 vcc, s97, v3
	s_nop 1
	v_cndmask_b32_e32 v7, v93, v7, vcc
	v_mul_f32_e32 v7, v7, v115
	global_store_dword v10, v7, s[44:45]
	v_add_f32_e64 v99, |v4|, |v7|
	s_add_u32 s44, s44, 0x10000
	s_addc_u32 s45, s45, 0
	v_add_f32_e32 v2, 0x41200000, v159
	v_fmamk_f32 v2, v2, 0x3e2119e2, v80
	v_mul_f32_e64 v3, |v2|, v77
	v_mul_f32_e32 v4, 0x3fb8aa3b, v3
	v_fma_f32 v5, v3, s95, -v4
	v_rndne_f32_e32 v6, v4
	v_fmac_f32_e32 v5, 0x32a5705f, v3
	v_sub_f32_e32 v4, v4, v6
	v_add_f32_e32 v4, v4, v5
	v_exp_f32_e32 v4, v4
	v_cvt_i32_f32_e32 v6, v6
	v_cmp_ngt_f32_e32 vcc, s96, v3
	v_ldexp_f32 v4, v4, v6
	s_nop 0
	v_cndmask_b32_e32 v4, 0, v4, vcc
	v_cmp_nlt_f32_e32 vcc, s97, v3
	s_nop 1
	v_cndmask_b32_e32 v4, v93, v4, vcc
	v_mul_f32_e32 v4, v4, v100
	global_store_dword v9, v4, s[44:45]
	v_mul_f32_e64 v3, |v2|, v158
	v_mul_f32_e32 v7, 0x3fb8aa3b, v3
	v_fma_f32 v5, v3, s95, -v7
	v_rndne_f32_e32 v6, v7
	v_fmac_f32_e32 v5, 0x32a5705f, v3
	v_sub_f32_e32 v7, v7, v6
	v_add_f32_e32 v7, v7, v5
	v_exp_f32_e32 v7, v7
	v_cvt_i32_f32_e32 v6, v6
	v_cmp_ngt_f32_e32 vcc, s96, v3
	v_ldexp_f32 v7, v7, v6
	s_nop 0
	v_cndmask_b32_e32 v7, 0, v7, vcc
	v_cmp_nlt_f32_e32 vcc, s97, v3
	s_nop 1
	v_cndmask_b32_e32 v7, v93, v7, vcc
	v_mul_f32_e32 v7, v7, v116
	global_store_dword v10, v7, s[44:45]
	v_add_f32_e64 v100, |v4|, |v7|
	s_add_u32 s44, s44, 0x10000
	s_addc_u32 s45, s45, 0
	v_add_f32_e32 v2, 0x41300000, v159
	v_fmamk_f32 v2, v2, 0x3e2119e2, v80
	v_mul_f32_e64 v3, |v2|, v77
	v_mul_f32_e32 v4, 0x3fb8aa3b, v3
	v_fma_f32 v5, v3, s95, -v4
	v_rndne_f32_e32 v6, v4
	v_fmac_f32_e32 v5, 0x32a5705f, v3
	v_sub_f32_e32 v4, v4, v6
	v_add_f32_e32 v4, v4, v5
	v_exp_f32_e32 v4, v4
	v_cvt_i32_f32_e32 v6, v6
	v_cmp_ngt_f32_e32 vcc, s96, v3
	v_ldexp_f32 v4, v4, v6
	s_nop 0
	v_cndmask_b32_e32 v4, 0, v4, vcc
	v_cmp_nlt_f32_e32 vcc, s97, v3
	s_nop 1
	v_cndmask_b32_e32 v4, v93, v4, vcc
	v_mul_f32_e32 v4, v4, v101
	global_store_dword v9, v4, s[44:45]
	v_mul_f32_e64 v3, |v2|, v158
	v_mul_f32_e32 v7, 0x3fb8aa3b, v3
	v_fma_f32 v5, v3, s95, -v7
	v_rndne_f32_e32 v6, v7
	v_fmac_f32_e32 v5, 0x32a5705f, v3
	v_sub_f32_e32 v7, v7, v6
	v_add_f32_e32 v7, v7, v5
	v_exp_f32_e32 v7, v7
	v_cvt_i32_f32_e32 v6, v6
	v_cmp_ngt_f32_e32 vcc, s96, v3
	v_ldexp_f32 v7, v7, v6
	s_nop 0
	v_cndmask_b32_e32 v7, 0, v7, vcc
	v_cmp_nlt_f32_e32 vcc, s97, v3
	s_nop 1
	v_cndmask_b32_e32 v7, v93, v7, vcc
	v_mul_f32_e32 v7, v7, v117
	global_store_dword v10, v7, s[44:45]
	v_add_f32_e64 v101, |v4|, |v7|
	s_add_u32 s44, s44, 0x50000
	s_addc_u32 s45, s45, 0
	v_add_f32_e32 v2, 0x41800000, v159
	v_fmamk_f32 v2, v2, 0x3e2119e2, v80
	v_mul_f32_e64 v3, |v2|, v77
	v_mul_f32_e32 v4, 0x3fb8aa3b, v3
	v_fma_f32 v5, v3, s95, -v4
	v_rndne_f32_e32 v6, v4
	v_fmac_f32_e32 v5, 0x32a5705f, v3
	v_sub_f32_e32 v4, v4, v6
	v_add_f32_e32 v4, v4, v5
	v_exp_f32_e32 v4, v4
	v_cvt_i32_f32_e32 v6, v6
	v_cmp_ngt_f32_e32 vcc, s96, v3
	v_ldexp_f32 v4, v4, v6
	s_nop 0
	v_cndmask_b32_e32 v4, 0, v4, vcc
	v_cmp_nlt_f32_e32 vcc, s97, v3
	s_nop 1
	v_cndmask_b32_e32 v4, v93, v4, vcc
	v_mul_f32_e32 v4, v4, v102
	global_store_dword v9, v4, s[44:45]
	v_mul_f32_e64 v3, |v2|, v158
	v_mul_f32_e32 v7, 0x3fb8aa3b, v3
	v_fma_f32 v5, v3, s95, -v7
	v_rndne_f32_e32 v6, v7
	v_fmac_f32_e32 v5, 0x32a5705f, v3
	v_sub_f32_e32 v7, v7, v6
	v_add_f32_e32 v7, v7, v5
	v_exp_f32_e32 v7, v7
	v_cvt_i32_f32_e32 v6, v6
	v_cmp_ngt_f32_e32 vcc, s96, v3
	v_ldexp_f32 v7, v7, v6
	s_nop 0
	v_cndmask_b32_e32 v7, 0, v7, vcc
	v_cmp_nlt_f32_e32 vcc, s97, v3
	s_nop 1
	v_cndmask_b32_e32 v7, v93, v7, vcc
	v_mul_f32_e32 v7, v7, v118
	global_store_dword v10, v7, s[44:45]
	v_add_f32_e64 v102, |v4|, |v7|
	s_add_u32 s44, s44, 0x10000
	s_addc_u32 s45, s45, 0
	v_add_f32_e32 v2, 0x41880000, v159
	v_fmamk_f32 v2, v2, 0x3e2119e2, v80
	v_mul_f32_e64 v3, |v2|, v77
	v_mul_f32_e32 v4, 0x3fb8aa3b, v3
	v_fma_f32 v5, v3, s95, -v4
	v_rndne_f32_e32 v6, v4
	v_fmac_f32_e32 v5, 0x32a5705f, v3
	v_sub_f32_e32 v4, v4, v6
	v_add_f32_e32 v4, v4, v5
	v_exp_f32_e32 v4, v4
	v_cvt_i32_f32_e32 v6, v6
	v_cmp_ngt_f32_e32 vcc, s96, v3
	v_ldexp_f32 v4, v4, v6
	s_nop 0
	v_cndmask_b32_e32 v4, 0, v4, vcc
	v_cmp_nlt_f32_e32 vcc, s97, v3
	s_nop 1
	v_cndmask_b32_e32 v4, v93, v4, vcc
	v_mul_f32_e32 v4, v4, v103
	global_store_dword v9, v4, s[44:45]
	v_mul_f32_e64 v3, |v2|, v158
	v_mul_f32_e32 v7, 0x3fb8aa3b, v3
	v_fma_f32 v5, v3, s95, -v7
	v_rndne_f32_e32 v6, v7
	v_fmac_f32_e32 v5, 0x32a5705f, v3
	v_sub_f32_e32 v7, v7, v6
	v_add_f32_e32 v7, v7, v5
	v_exp_f32_e32 v7, v7
	v_cvt_i32_f32_e32 v6, v6
	v_cmp_ngt_f32_e32 vcc, s96, v3
	v_ldexp_f32 v7, v7, v6
	s_nop 0
	v_cndmask_b32_e32 v7, 0, v7, vcc
	v_cmp_nlt_f32_e32 vcc, s97, v3
	s_nop 1
	v_cndmask_b32_e32 v7, v93, v7, vcc
	v_mul_f32_e32 v7, v7, v119
	global_store_dword v10, v7, s[44:45]
	v_add_f32_e64 v103, |v4|, |v7|
	s_add_u32 s44, s44, 0x10000
	s_addc_u32 s45, s45, 0
	v_add_f32_e32 v2, 0x41900000, v159
	v_fmamk_f32 v2, v2, 0x3e2119e2, v80
	v_mul_f32_e64 v3, |v2|, v77
	v_mul_f32_e32 v4, 0x3fb8aa3b, v3
	v_fma_f32 v5, v3, s95, -v4
	v_rndne_f32_e32 v6, v4
	v_fmac_f32_e32 v5, 0x32a5705f, v3
	v_sub_f32_e32 v4, v4, v6
	v_add_f32_e32 v4, v4, v5
	v_exp_f32_e32 v4, v4
	v_cvt_i32_f32_e32 v6, v6
	v_cmp_ngt_f32_e32 vcc, s96, v3
	v_ldexp_f32 v4, v4, v6
	s_nop 0
	v_cndmask_b32_e32 v4, 0, v4, vcc
	v_cmp_nlt_f32_e32 vcc, s97, v3
	s_nop 1
	v_cndmask_b32_e32 v4, v93, v4, vcc
	v_mul_f32_e32 v4, v4, v104
	global_store_dword v9, v4, s[44:45]
	v_mul_f32_e64 v3, |v2|, v158
	v_mul_f32_e32 v7, 0x3fb8aa3b, v3
	v_fma_f32 v5, v3, s95, -v7
	v_rndne_f32_e32 v6, v7
	v_fmac_f32_e32 v5, 0x32a5705f, v3
	v_sub_f32_e32 v7, v7, v6
	v_add_f32_e32 v7, v7, v5
	v_exp_f32_e32 v7, v7
	v_cvt_i32_f32_e32 v6, v6
	v_cmp_ngt_f32_e32 vcc, s96, v3
	v_ldexp_f32 v7, v7, v6
	s_nop 0
	v_cndmask_b32_e32 v7, 0, v7, vcc
	v_cmp_nlt_f32_e32 vcc, s97, v3
	s_nop 1
	v_cndmask_b32_e32 v7, v93, v7, vcc
	v_mul_f32_e32 v7, v7, v120
	global_store_dword v10, v7, s[44:45]
	v_add_f32_e64 v104, |v4|, |v7|
	s_add_u32 s44, s44, 0x10000
	s_addc_u32 s45, s45, 0
	v_add_f32_e32 v2, 0x41980000, v159
	v_fmamk_f32 v2, v2, 0x3e2119e2, v80
	v_mul_f32_e64 v3, |v2|, v77
	v_mul_f32_e32 v4, 0x3fb8aa3b, v3
	v_fma_f32 v5, v3, s95, -v4
	v_rndne_f32_e32 v6, v4
	v_fmac_f32_e32 v5, 0x32a5705f, v3
	v_sub_f32_e32 v4, v4, v6
	v_add_f32_e32 v4, v4, v5
	v_exp_f32_e32 v4, v4
	v_cvt_i32_f32_e32 v6, v6
	v_cmp_ngt_f32_e32 vcc, s96, v3
	v_ldexp_f32 v4, v4, v6
	s_nop 0
	v_cndmask_b32_e32 v4, 0, v4, vcc
	v_cmp_nlt_f32_e32 vcc, s97, v3
	s_nop 1
	v_cndmask_b32_e32 v4, v93, v4, vcc
	v_mul_f32_e32 v4, v4, v105
	global_store_dword v9, v4, s[44:45]
	v_mul_f32_e64 v3, |v2|, v158
	v_mul_f32_e32 v7, 0x3fb8aa3b, v3
	v_fma_f32 v5, v3, s95, -v7
	v_rndne_f32_e32 v6, v7
	v_fmac_f32_e32 v5, 0x32a5705f, v3
	v_sub_f32_e32 v7, v7, v6
	v_add_f32_e32 v7, v7, v5
	v_exp_f32_e32 v7, v7
	v_cvt_i32_f32_e32 v6, v6
	v_cmp_ngt_f32_e32 vcc, s96, v3
	v_ldexp_f32 v7, v7, v6
	s_nop 0
	v_cndmask_b32_e32 v7, 0, v7, vcc
	v_cmp_nlt_f32_e32 vcc, s97, v3
	s_nop 1
	v_cndmask_b32_e32 v7, v93, v7, vcc
	v_mul_f32_e32 v7, v7, v121
	global_store_dword v10, v7, s[44:45]
	v_add_f32_e64 v105, |v4|, |v7|
	s_add_u32 s44, s44, 0x50000
	s_addc_u32 s45, s45, 0
	v_add_f32_e32 v2, 0x41c00000, v159
	v_fmamk_f32 v2, v2, 0x3e2119e2, v80
	v_mul_f32_e64 v3, |v2|, v77
	v_mul_f32_e32 v4, 0x3fb8aa3b, v3
	v_fma_f32 v5, v3, s95, -v4
	v_rndne_f32_e32 v6, v4
	v_fmac_f32_e32 v5, 0x32a5705f, v3
	v_sub_f32_e32 v4, v4, v6
	v_add_f32_e32 v4, v4, v5
	v_exp_f32_e32 v4, v4
	v_cvt_i32_f32_e32 v6, v6
	v_cmp_ngt_f32_e32 vcc, s96, v3
	v_ldexp_f32 v4, v4, v6
	s_nop 0
	v_cndmask_b32_e32 v4, 0, v4, vcc
	v_cmp_nlt_f32_e32 vcc, s97, v3
	s_nop 1
	v_cndmask_b32_e32 v4, v93, v4, vcc
	v_mul_f32_e32 v4, v4, v106
	global_store_dword v9, v4, s[44:45]
	v_mul_f32_e64 v3, |v2|, v158
	v_mul_f32_e32 v7, 0x3fb8aa3b, v3
	v_fma_f32 v5, v3, s95, -v7
	v_rndne_f32_e32 v6, v7
	v_fmac_f32_e32 v5, 0x32a5705f, v3
	v_sub_f32_e32 v7, v7, v6
	v_add_f32_e32 v7, v7, v5
	v_exp_f32_e32 v7, v7
	v_cvt_i32_f32_e32 v6, v6
	v_cmp_ngt_f32_e32 vcc, s96, v3
	v_ldexp_f32 v7, v7, v6
	s_nop 0
	v_cndmask_b32_e32 v7, 0, v7, vcc
	v_cmp_nlt_f32_e32 vcc, s97, v3
	s_nop 1
	v_cndmask_b32_e32 v7, v93, v7, vcc
	v_mul_f32_e32 v7, v7, v122
	global_store_dword v10, v7, s[44:45]
	v_add_f32_e64 v106, |v4|, |v7|
	s_add_u32 s44, s44, 0x10000
	s_addc_u32 s45, s45, 0
	v_add_f32_e32 v2, 0x41c80000, v159
	v_fmamk_f32 v2, v2, 0x3e2119e2, v80
	v_mul_f32_e64 v3, |v2|, v77
	v_mul_f32_e32 v4, 0x3fb8aa3b, v3
	v_fma_f32 v5, v3, s95, -v4
	v_rndne_f32_e32 v6, v4
	v_fmac_f32_e32 v5, 0x32a5705f, v3
	v_sub_f32_e32 v4, v4, v6
	v_add_f32_e32 v4, v4, v5
	v_exp_f32_e32 v4, v4
	v_cvt_i32_f32_e32 v6, v6
	v_cmp_ngt_f32_e32 vcc, s96, v3
	v_ldexp_f32 v4, v4, v6
	s_nop 0
	v_cndmask_b32_e32 v4, 0, v4, vcc
	v_cmp_nlt_f32_e32 vcc, s97, v3
	s_nop 1
	v_cndmask_b32_e32 v4, v93, v4, vcc
	v_mul_f32_e32 v4, v4, v107
	global_store_dword v9, v4, s[44:45]
	v_mul_f32_e64 v3, |v2|, v158
	v_mul_f32_e32 v7, 0x3fb8aa3b, v3
	v_fma_f32 v5, v3, s95, -v7
	v_rndne_f32_e32 v6, v7
	v_fmac_f32_e32 v5, 0x32a5705f, v3
	v_sub_f32_e32 v7, v7, v6
	v_add_f32_e32 v7, v7, v5
	v_exp_f32_e32 v7, v7
	v_cvt_i32_f32_e32 v6, v6
	v_cmp_ngt_f32_e32 vcc, s96, v3
	v_ldexp_f32 v7, v7, v6
	s_nop 0
	v_cndmask_b32_e32 v7, 0, v7, vcc
	v_cmp_nlt_f32_e32 vcc, s97, v3
	s_nop 1
	v_cndmask_b32_e32 v7, v93, v7, vcc
	v_mul_f32_e32 v7, v7, v123
	global_store_dword v10, v7, s[44:45]
	v_add_f32_e64 v107, |v4|, |v7|
	s_add_u32 s44, s44, 0x10000
	s_addc_u32 s45, s45, 0
	v_add_f32_e32 v2, 0x41d00000, v159
	v_fmamk_f32 v2, v2, 0x3e2119e2, v80
	v_mul_f32_e64 v3, |v2|, v77
	v_mul_f32_e32 v4, 0x3fb8aa3b, v3
	v_fma_f32 v5, v3, s95, -v4
	v_rndne_f32_e32 v6, v4
	v_fmac_f32_e32 v5, 0x32a5705f, v3
	v_sub_f32_e32 v4, v4, v6
	v_add_f32_e32 v4, v4, v5
	v_exp_f32_e32 v4, v4
	v_cvt_i32_f32_e32 v6, v6
	v_cmp_ngt_f32_e32 vcc, s96, v3
	v_ldexp_f32 v4, v4, v6
	s_nop 0
	v_cndmask_b32_e32 v4, 0, v4, vcc
	v_cmp_nlt_f32_e32 vcc, s97, v3
	s_nop 1
	v_cndmask_b32_e32 v4, v93, v4, vcc
	v_mul_f32_e32 v4, v4, v108
	global_store_dword v9, v4, s[44:45]
	v_mul_f32_e64 v3, |v2|, v158
	v_mul_f32_e32 v7, 0x3fb8aa3b, v3
	v_fma_f32 v5, v3, s95, -v7
	v_rndne_f32_e32 v6, v7
	v_fmac_f32_e32 v5, 0x32a5705f, v3
	v_sub_f32_e32 v7, v7, v6
	v_add_f32_e32 v7, v7, v5
	v_exp_f32_e32 v7, v7
	v_cvt_i32_f32_e32 v6, v6
	v_cmp_ngt_f32_e32 vcc, s96, v3
	v_ldexp_f32 v7, v7, v6
	s_nop 0
	v_cndmask_b32_e32 v7, 0, v7, vcc
	v_cmp_nlt_f32_e32 vcc, s97, v3
	s_nop 1
	v_cndmask_b32_e32 v7, v93, v7, vcc
	v_mul_f32_e32 v7, v7, v124
	global_store_dword v10, v7, s[44:45]
	v_add_f32_e64 v108, |v4|, |v7|
	s_add_u32 s44, s44, 0x10000
	s_addc_u32 s45, s45, 0
	v_add_f32_e32 v2, 0x41d80000, v159
	v_fmamk_f32 v2, v2, 0x3e2119e2, v80
	v_mul_f32_e64 v3, |v2|, v77
	v_mul_f32_e32 v4, 0x3fb8aa3b, v3
	v_fma_f32 v5, v3, s95, -v4
	v_rndne_f32_e32 v6, v4
	v_fmac_f32_e32 v5, 0x32a5705f, v3
	v_sub_f32_e32 v4, v4, v6
	v_add_f32_e32 v4, v4, v5
	v_exp_f32_e32 v4, v4
	v_cvt_i32_f32_e32 v6, v6
	v_cmp_ngt_f32_e32 vcc, s96, v3
	v_ldexp_f32 v4, v4, v6
	s_nop 0
	v_cndmask_b32_e32 v4, 0, v4, vcc
	v_cmp_nlt_f32_e32 vcc, s97, v3
	s_nop 1
	v_cndmask_b32_e32 v4, v93, v4, vcc
	v_mul_f32_e32 v4, v4, v109
	global_store_dword v9, v4, s[44:45]
	v_mul_f32_e64 v3, |v2|, v158
	v_mul_f32_e32 v7, 0x3fb8aa3b, v3
	v_fma_f32 v5, v3, s95, -v7
	v_rndne_f32_e32 v6, v7
	v_fmac_f32_e32 v5, 0x32a5705f, v3
	v_sub_f32_e32 v7, v7, v6
	v_add_f32_e32 v7, v7, v5
	v_exp_f32_e32 v7, v7
	v_cvt_i32_f32_e32 v6, v6
	v_cmp_ngt_f32_e32 vcc, s96, v3
	v_ldexp_f32 v7, v7, v6
	s_nop 0
	v_cndmask_b32_e32 v7, 0, v7, vcc
	v_cmp_nlt_f32_e32 vcc, s97, v3
	s_nop 1
	v_cndmask_b32_e32 v7, v93, v7, vcc
	v_mul_f32_e32 v7, v7, v125
	global_store_dword v10, v7, s[44:45]
	v_add_f32_e64 v109, |v4|, |v7|
	v_add_f32_dpp v94, v94, v94 row_shr:1 row_mask:0xf bank_mask:0xf
	v_add_f32_dpp v95, v95, v95 row_shr:1 row_mask:0xf bank_mask:0xf
	v_add_f32_dpp v96, v96, v96 row_shr:1 row_mask:0xf bank_mask:0xf
	v_add_f32_dpp v97, v97, v97 row_shr:1 row_mask:0xf bank_mask:0xf
	v_add_f32_dpp v98, v98, v98 row_shr:1 row_mask:0xf bank_mask:0xf
	v_add_f32_dpp v99, v99, v99 row_shr:1 row_mask:0xf bank_mask:0xf
	v_add_f32_dpp v100, v100, v100 row_shr:1 row_mask:0xf bank_mask:0xf
	v_add_f32_dpp v101, v101, v101 row_shr:1 row_mask:0xf bank_mask:0xf
	v_add_f32_dpp v102, v102, v102 row_shr:1 row_mask:0xf bank_mask:0xf
	v_add_f32_dpp v103, v103, v103 row_shr:1 row_mask:0xf bank_mask:0xf
	v_add_f32_dpp v104, v104, v104 row_shr:1 row_mask:0xf bank_mask:0xf
	v_add_f32_dpp v105, v105, v105 row_shr:1 row_mask:0xf bank_mask:0xf
	v_add_f32_dpp v106, v106, v106 row_shr:1 row_mask:0xf bank_mask:0xf
	v_add_f32_dpp v107, v107, v107 row_shr:1 row_mask:0xf bank_mask:0xf
	v_add_f32_dpp v108, v108, v108 row_shr:1 row_mask:0xf bank_mask:0xf
	v_add_f32_dpp v109, v109, v109 row_shr:1 row_mask:0xf bank_mask:0xf
	v_add_f32_dpp v94, v94, v94 row_shr:2 row_mask:0xf bank_mask:0xf
	v_add_f32_dpp v95, v95, v95 row_shr:2 row_mask:0xf bank_mask:0xf
	v_add_f32_dpp v96, v96, v96 row_shr:2 row_mask:0xf bank_mask:0xf
	v_add_f32_dpp v97, v97, v97 row_shr:2 row_mask:0xf bank_mask:0xf
	v_add_f32_dpp v98, v98, v98 row_shr:2 row_mask:0xf bank_mask:0xf
	v_add_f32_dpp v99, v99, v99 row_shr:2 row_mask:0xf bank_mask:0xf
	v_add_f32_dpp v100, v100, v100 row_shr:2 row_mask:0xf bank_mask:0xf
	v_add_f32_dpp v101, v101, v101 row_shr:2 row_mask:0xf bank_mask:0xf
	v_add_f32_dpp v102, v102, v102 row_shr:2 row_mask:0xf bank_mask:0xf
	v_add_f32_dpp v103, v103, v103 row_shr:2 row_mask:0xf bank_mask:0xf
	v_add_f32_dpp v104, v104, v104 row_shr:2 row_mask:0xf bank_mask:0xf
	v_add_f32_dpp v105, v105, v105 row_shr:2 row_mask:0xf bank_mask:0xf
	v_add_f32_dpp v106, v106, v106 row_shr:2 row_mask:0xf bank_mask:0xf
	v_add_f32_dpp v107, v107, v107 row_shr:2 row_mask:0xf bank_mask:0xf
	v_add_f32_dpp v108, v108, v108 row_shr:2 row_mask:0xf bank_mask:0xf
	v_add_f32_dpp v109, v109, v109 row_shr:2 row_mask:0xf bank_mask:0xf
	v_add_f32_dpp v94, v94, v94 row_shr:4 row_mask:0xf bank_mask:0xf
	v_add_f32_dpp v95, v95, v95 row_shr:4 row_mask:0xf bank_mask:0xf
	v_add_f32_dpp v96, v96, v96 row_shr:4 row_mask:0xf bank_mask:0xf
	v_add_f32_dpp v97, v97, v97 row_shr:4 row_mask:0xf bank_mask:0xf
	v_add_f32_dpp v98, v98, v98 row_shr:4 row_mask:0xf bank_mask:0xf
	v_add_f32_dpp v99, v99, v99 row_shr:4 row_mask:0xf bank_mask:0xf
	v_add_f32_dpp v100, v100, v100 row_shr:4 row_mask:0xf bank_mask:0xf
	v_add_f32_dpp v101, v101, v101 row_shr:4 row_mask:0xf bank_mask:0xf
	v_add_f32_dpp v102, v102, v102 row_shr:4 row_mask:0xf bank_mask:0xf
	v_add_f32_dpp v103, v103, v103 row_shr:4 row_mask:0xf bank_mask:0xf
	v_add_f32_dpp v104, v104, v104 row_shr:4 row_mask:0xf bank_mask:0xf
	v_add_f32_dpp v105, v105, v105 row_shr:4 row_mask:0xf bank_mask:0xf
	v_add_f32_dpp v106, v106, v106 row_shr:4 row_mask:0xf bank_mask:0xf
	v_add_f32_dpp v107, v107, v107 row_shr:4 row_mask:0xf bank_mask:0xf
	v_add_f32_dpp v108, v108, v108 row_shr:4 row_mask:0xf bank_mask:0xf
	v_add_f32_dpp v109, v109, v109 row_shr:4 row_mask:0xf bank_mask:0xf
	v_add_f32_dpp v94, v94, v94 row_shr:8 row_mask:0xf bank_mask:0xf
	v_add_f32_dpp v95, v95, v95 row_shr:8 row_mask:0xf bank_mask:0xf
	v_add_f32_dpp v96, v96, v96 row_shr:8 row_mask:0xf bank_mask:0xf
	v_add_f32_dpp v97, v97, v97 row_shr:8 row_mask:0xf bank_mask:0xf
	v_add_f32_dpp v98, v98, v98 row_shr:8 row_mask:0xf bank_mask:0xf
	v_add_f32_dpp v99, v99, v99 row_shr:8 row_mask:0xf bank_mask:0xf
	v_add_f32_dpp v100, v100, v100 row_shr:8 row_mask:0xf bank_mask:0xf
	v_add_f32_dpp v101, v101, v101 row_shr:8 row_mask:0xf bank_mask:0xf
	v_add_f32_dpp v102, v102, v102 row_shr:8 row_mask:0xf bank_mask:0xf
	v_add_f32_dpp v103, v103, v103 row_shr:8 row_mask:0xf bank_mask:0xf
	v_add_f32_dpp v104, v104, v104 row_shr:8 row_mask:0xf bank_mask:0xf
	v_add_f32_dpp v105, v105, v105 row_shr:8 row_mask:0xf bank_mask:0xf
	v_add_f32_dpp v106, v106, v106 row_shr:8 row_mask:0xf bank_mask:0xf
	v_add_f32_dpp v107, v107, v107 row_shr:8 row_mask:0xf bank_mask:0xf
	v_add_f32_dpp v108, v108, v108 row_shr:8 row_mask:0xf bank_mask:0xf
	v_add_f32_dpp v109, v109, v109 row_shr:8 row_mask:0xf bank_mask:0xf
	v_add_f32_dpp v94, v94, v94 row_bcast:15 row_mask:0xa bank_mask:0xf
	v_add_f32_dpp v95, v95, v95 row_bcast:15 row_mask:0xa bank_mask:0xf
	v_add_f32_dpp v96, v96, v96 row_bcast:15 row_mask:0xa bank_mask:0xf
	v_add_f32_dpp v97, v97, v97 row_bcast:15 row_mask:0xa bank_mask:0xf
	v_add_f32_dpp v98, v98, v98 row_bcast:15 row_mask:0xa bank_mask:0xf
	v_add_f32_dpp v99, v99, v99 row_bcast:15 row_mask:0xa bank_mask:0xf
	v_add_f32_dpp v100, v100, v100 row_bcast:15 row_mask:0xa bank_mask:0xf
	v_add_f32_dpp v101, v101, v101 row_bcast:15 row_mask:0xa bank_mask:0xf
	v_add_f32_dpp v102, v102, v102 row_bcast:15 row_mask:0xa bank_mask:0xf
	v_add_f32_dpp v103, v103, v103 row_bcast:15 row_mask:0xa bank_mask:0xf
	v_add_f32_dpp v104, v104, v104 row_bcast:15 row_mask:0xa bank_mask:0xf
	v_add_f32_dpp v105, v105, v105 row_bcast:15 row_mask:0xa bank_mask:0xf
	v_add_f32_dpp v106, v106, v106 row_bcast:15 row_mask:0xa bank_mask:0xf
	v_add_f32_dpp v107, v107, v107 row_bcast:15 row_mask:0xa bank_mask:0xf
	v_add_f32_dpp v108, v108, v108 row_bcast:15 row_mask:0xa bank_mask:0xf
	v_add_f32_dpp v109, v109, v109 row_bcast:15 row_mask:0xa bank_mask:0xf
	s_mov_b32 s46, s28
	s_mov_b32 s47, s29
	s_mov_b64 exec, s[34:35]
	global_store_dword v76, v94, s[46:47]
	s_add_u32 s46, s46, 0x400
	s_addc_u32 s47, s47, 0
	global_store_dword v76, v95, s[46:47]
	s_add_u32 s46, s46, 0x400
	s_addc_u32 s47, s47, 0
	global_store_dword v76, v96, s[46:47]
	s_add_u32 s46, s46, 0x400
	s_addc_u32 s47, s47, 0
	global_store_dword v76, v97, s[46:47]
	s_add_u32 s46, s46, 0x1400
	s_addc_u32 s47, s47, 0
	global_store_dword v76, v98, s[46:47]
	s_add_u32 s46, s46, 0x400
	s_addc_u32 s47, s47, 0
	global_store_dword v76, v99, s[46:47]
	s_add_u32 s46, s46, 0x400
	s_addc_u32 s47, s47, 0
	global_store_dword v76, v100, s[46:47]
	s_add_u32 s46, s46, 0x400
	s_addc_u32 s47, s47, 0
	global_store_dword v76, v101, s[46:47]
	s_add_u32 s46, s46, 0x1400
	s_addc_u32 s47, s47, 0
	global_store_dword v76, v102, s[46:47]
	s_add_u32 s46, s46, 0x400
	s_addc_u32 s47, s47, 0
	global_store_dword v76, v103, s[46:47]
	s_add_u32 s46, s46, 0x400
	s_addc_u32 s47, s47, 0
	global_store_dword v76, v104, s[46:47]
	s_add_u32 s46, s46, 0x400
	s_addc_u32 s47, s47, 0
	global_store_dword v76, v105, s[46:47]
	s_add_u32 s46, s46, 0x1400
	s_addc_u32 s47, s47, 0
	global_store_dword v76, v106, s[46:47]
	s_add_u32 s46, s46, 0x400
	s_addc_u32 s47, s47, 0
	global_store_dword v76, v107, s[46:47]
	s_add_u32 s46, s46, 0x400
	s_addc_u32 s47, s47, 0
	global_store_dword v76, v108, s[46:47]
	s_add_u32 s46, s46, 0x400
	s_addc_u32 s47, s47, 0
	global_store_dword v76, v109, s[46:47]
	s_mov_b64 exec, -1
	s_add_u32 s26, s26, 0x200000
	s_addc_u32 s27, s27, 0
	s_add_u32 s28, s28, 0x8000
	s_addc_u32 s29, s29, 0
	v_add_f32_e32 v159, 0x42000000, v159
	s_add_i32 s30, s30, 1
	s_waitcnt vmcnt(48)
	s_cmp_lt_u32 s30, 4
	s_cbranch_scc1 .Lhf_blk
	s_barrier
	s_branch .LBB0_6
